# speedup vs baseline: 1.0426x; 1.0426x over previous
_Z11knrm_kernelPKfS0_PKiS2_S0_Pf:
	s_load_dwordx8 s[4:11], s[0:1], 0x0
	s_load_dwordx4 s[12:15], s[0:1], 0x20
	v_lshrrev_b32_e32 v1, 6, v0
	v_and_b32_e32 v120, 63, v0
	v_lshrrev_b32_e32 v100, 4, v0
	v_and_b32_e32 v123, 15, v0
	v_lshlrev_b32_e32 v124, 5, v1
	s_lshl_b32 s3, s2, 5
	v_lshl_or_b32 v8, s2, 8, v124
	v_or_b32_e32 v2, s3, v100
	s_movk_i32 s3, 0x4b0
	v_mul_lo_u32 v2, v2, s3
	v_mul_lo_u32 v99, v8, s3
	v_lshlrev_b32_e32 v132, 4, v120
	v_min_u32_e32 v193, 23, v120
	v_lshl_add_u32 v3, v123, 4, v2
	v_min_u32_e32 v4, 10, v123
	v_add_u32_e32 v192, v99, v132
	v_lshlrev_b32_e32 v193, 4, v193
	s_movk_i32 s27, 0x1000
	s_movk_i32 s28, 0x2000
	v_lshl_add_u32 v2, v4, 4, v2
	v_add3_u32 v193, v99, v193, s28
	s_mov_b32 s19, 0x20000
	s_mov_b32 s18, 0x4b00000
	s_waitcnt lgkmcnt(0)
	s_mov_b64 s[16:17], s[6:7]
	s_and_b32 s5, s5, 0xffff
	s_mov_b32 s6, 0x960000
	s_mov_b32 s7, s19
	s_and_b32 s17, s17, 0xffff
	buffer_load_dwordx4 v[90:93], v3, s[4:7], 0 offen nt
	buffer_load_dwordx4 v[86:89], v3, s[4:7], 0 offen offset:256 nt
	buffer_load_dwordx4 v[82:85], v3, s[4:7], 0 offen offset:512 nt
	buffer_load_dwordx4 v[78:81], v3, s[4:7], 0 offen offset:768 nt
	buffer_load_dwordx4 v[94:97], v2, s[4:7], 0 offen offset:1024 nt
	buffer_load_dwordx4 v[2:5], v192, s[16:19], 0 offen nt
	buffer_load_dwordx4 v[14:17], v192, s[16:19], 0 offen offset:1024 nt
	buffer_load_dwordx4 v[34:37], v192, s[16:19], 0 offen offset:2048 nt
	buffer_load_dwordx4 v[46:49], v192, s[16:19], 0 offen offset:3072 nt
	buffer_load_dwordx4 v[54:57], v192, s[16:19], s27 offen nt
	buffer_load_dwordx4 v[58:61], v192, s[16:19], s27 offen offset:1024 nt
	buffer_load_dwordx4 v[62:65], v192, s[16:19], s27 offen offset:2048 nt
	buffer_load_dwordx4 v[66:69], v192, s[16:19], s27 offen offset:3072 nt
	buffer_load_dwordx4 v[70:73], v192, s[16:19], s28 offen nt
	buffer_load_dwordx4 v[74:77], v193, s[16:19], 0 offen offset:1024 nt
	v_lshlrev_b32_e32 v42, 2, v0
	v_bfe_u32 v43, v0, 2, 2
	v_and_or_b32 v98, v42, 12, v43
	v_and_or_b32 v6, v98, 7, v8
	v_ashrrev_i32_e32 v7, 31, v6
	s_movk_i32 s0, 0x160
	v_lshl_add_u64 v[6:7], v[6:7], 2, s[10:11]
	v_lshrrev_b32_e32 v121, 5, v0
	v_cmp_gt_u32_e64 s[0:1], s0, v0
	global_load_dword v125, v[6:7], off
	global_load_dword v126, v[6:7], off offset:64
	global_load_dword v127, v[6:7], off offset:96
	global_load_dword v190, v[6:7], off offset:32
	v_cndmask_b32_e64 v42, 10, v121, s[0:1]
	v_lshlrev_b32_e32 v42, 2, v42
	s_lshl_b32 s3, s2, 5
	v_and_b32_e32 v122, 31, v0
	global_load_dword v118, v42, s[12:13]
	v_or_b32_e32 v42, s3, v122
	v_ashrrev_i32_e32 v43, 31, v42
	v_lshl_add_u64 v[42:43], v[42:43], 2, s[8:9]
	global_load_dword v119, v[42:43], off
	s_mov_b32 s3, 0
	v_mul_u32_u24_e32 v131, 0x2600, v1
	v_lshl_add_u32 v141, v120, 3, v131
	v_add_u32_e32 v194, 64, v120
	v_mul_u32_u24_e32 v195, 0x1b5, v194
	v_lshrrev_b32_e32 v195, 15, v195
	v_add_u32_e32 v194, v194, v195
	v_lshl_add_u32 v143, v194, 3, v131
	v_add_u32_e32 v194, 128, v120
	v_mul_u32_u24_e32 v195, 0x1b5, v194
	v_lshrrev_b32_e32 v195, 15, v195
	v_add_u32_e32 v194, v194, v195
	v_lshl_add_u32 v144, v194, 3, v131
	v_add_u32_e32 v194, 192, v120
	v_mul_u32_u24_e32 v195, 0x1b5, v194
	v_lshrrev_b32_e32 v195, 15, v195
	v_add_u32_e32 v194, v194, v195
	v_lshl_add_u32 v145, v194, 3, v131
	v_add_u32_e32 v194, 256, v120
	v_mul_u32_u24_e32 v195, 0x1b5, v194
	v_lshrrev_b32_e32 v195, 15, v195
	v_add_u32_e32 v194, v194, v195
	v_lshl_add_u32 v146, v194, 3, v131
	v_add_u32_e32 v194, 320, v120
	v_mul_u32_u24_e32 v195, 0x1b5, v194
	v_lshrrev_b32_e32 v195, 15, v195
	v_add_u32_e32 v194, v194, v195
	v_lshl_add_u32 v147, v194, 3, v131
	v_add_u32_e32 v194, 448, v120
	v_mul_u32_u24_e32 v195, 0x1b5, v194
	v_lshrrev_b32_e32 v195, 15, v195
	v_add_u32_e32 v194, v194, v195
	v_lshl_add_u32 v148, v194, 3, v131
	v_add_u32_e32 v194, 512, v120
	v_mul_u32_u24_e32 v195, 0x1b5, v194
	v_lshrrev_b32_e32 v195, 15, v195
	v_add_u32_e32 v194, v194, v195
	v_lshl_add_u32 v149, v194, 3, v131
	v_add_u32_e32 v194, 576, v120
	v_mul_u32_u24_e32 v195, 0x1b5, v194
	v_lshrrev_b32_e32 v195, 15, v195
	v_add_u32_e32 v194, v194, v195
	v_lshl_add_u32 v150, v194, 3, v131
	v_and_b32_e32 v196, 48, v120
	v_mul_u32_u24_e32 v197, 0x260, v123
	v_mul_u32_u24_e32 v198, 0x260, v98
	v_lshrrev_b32_e32 v199, 1, v120
	v_lshlrev_b32_e32 v200, 7, v1
	v_add_u32_e32 v136, v197, v196
	v_add_u32_e32 v198, v198, v131
	v_and_b32_e32 v199, 24, v199
	v_add_u32_e32 v200, 0x17c00, v200
	v_add_u32_e32 v142, v198, v196
	v_add_u32_e32 v159, v198, v199
	v_add3_u32 v160, v197, v199, 64
	v_lshl_add_u32 v139, v120, 2, v200
	v_add_u32_e32 v140, v200, v196
	v_add_u32_e32 v142, 0x4c00, v142
	v_cmp_gt_u32_e64 s[4:5], 16, v120
	s_and_saveexec_b64 s[6:7], s[4:5]
	s_movk_i32 s8, 0x260
	v_mov_b32_e32 v102, 0
	v_mad_u32_u24 v101, v120, s8, v131
	v_mov_b32_e32 v103, v102
	ds_write_b64 v101, v[102:103] offset:20056
	s_or_b64 exec, exec, s[6:7]
	v_cmp_lt_u32_e32 vcc, 10, v123
	s_waitcnt vmcnt(19)
	v_mul_f32_e32 v101, v87, v87
	v_mov_b32_e32 v106, v92
	s_waitcnt vmcnt(16)
	v_cndmask_b32_e64 v103, v97, 0, vcc
	v_cndmask_b32_e64 v102, v96, 0, vcc
	v_mov_b32_e32 v96, v91
	v_mov_b32_e32 v97, v83
	v_cndmask_b32_e64 v105, v95, 0, vcc
	v_cndmask_b32_e64 v104, v94, 0, vcc
	v_mov_b32_e32 v94, v90
	v_mov_b32_e32 v95, v82
	v_pk_mul_f32 v[96:97], v[96:97], v[96:97]
	v_mov_b32_e32 v107, v84
	v_fmac_f32_e32 v101, v86, v86
	v_pk_fma_f32 v[94:95], v[94:95], v[94:95], v[96:97]
	v_mov_b32_e32 v108, v93
	v_mov_b32_e32 v109, v85
	v_fmac_f32_e32 v101, v88, v88
	v_pk_fma_f32 v[94:95], v[106:107], v[106:107], v[94:95]
	v_fmac_f32_e32 v101, v89, v89
	v_pk_fma_f32 v[94:95], v[108:109], v[108:109], v[94:95]
	v_mov_b32_e32 v96, v79
	v_add_f32_e32 v94, v94, v101
	v_mov_b32_e32 v97, v105
	v_add_f32_e32 v101, v94, v95
	v_mov_b32_e32 v94, v78
	v_mov_b32_e32 v95, v104
	v_pk_mul_f32 v[96:97], v[96:97], v[96:97]
	s_mov_b32 s21, 0xf800000
	v_pk_fma_f32 v[94:95], v[94:95], v[94:95], v[96:97]
	v_mov_b32_e32 v96, v80
	v_mov_b32_e32 v97, v102
	v_pk_fma_f32 v[94:95], v[96:97], v[96:97], v[94:95]
	v_mov_b32_e32 v96, v81
	v_mov_b32_e32 v97, v103
	v_pk_fma_f32 v[94:95], v[96:97], v[96:97], v[94:95]
	v_mov_b32_e32 v135, 0x260
	v_add_f32_e32 v94, v101, v94
	v_add_f32_e32 v94, v94, v95
	v_mbcnt_lo_u32_b32 v95, -1, 0
	v_mbcnt_hi_u32_b32 v95, -1, v95
	v_and_b32_e32 v97, 64, v95
	v_add_u32_e32 v101, 64, v97
	s_movk_i32 s8, 0x260
	v_add_u32_e32 v137, 0x4b00, v99
	s_movk_i32 s10, 0x1b5
	v_mov_b32_e32 v99, 0x36a00
	v_mov_b32_e32 v111, 0x666c0
	v_mov_b32_e32 v113, 0x6d400
	v_mov_b32_e32 v115, 0x74140
	s_mov_b32 s20, 0xbeb17218
	s_mov_b32 s22, 0x44132d1f
	v_mov_b32_e32 v161, 0xc47a0000
	v_add_f32_dpp v96, v94, v94 quad_perm:[1,0,3,2] row_mask:0xf bank_mask:0xf
	s_nop 1
	v_add_f32_dpp v94, v96, v96 quad_perm:[2,3,0,1] row_mask:0xf bank_mask:0xf
	s_nop 1
	v_add_f32_dpp v96, v94, v94 row_half_mirror row_mask:0xf bank_mask:0xf
	s_nop 1
	v_add_f32_dpp v94, v96, v96 row_mirror row_mask:0xf bank_mask:0xf
	v_mul_f32_e32 v96, 0x4f800000, v94
	v_cmp_gt_f32_e32 vcc, s21, v94
	s_nop 1
	v_cndmask_b32_e32 v94, v94, v96, vcc
	v_sqrt_f32_e32 v96, v94
	s_nop 0
	v_add_u32_e32 v106, -1, v96
	v_fma_f32 v107, -v106, v96, v94
	v_cmp_ge_f32_e64 s[6:7], 0, v107
	v_add_u32_e32 v107, 1, v96
	s_nop 0
	v_cndmask_b32_e64 v106, v96, v106, s[6:7]
	v_fma_f32 v96, -v107, v96, v94
	v_cmp_lt_f32_e64 s[6:7], 0, v96
	s_nop 1
	v_cndmask_b32_e64 v96, v106, v107, s[6:7]
	v_mul_f32_e32 v106, 0x37800000, v96
	v_cndmask_b32_e32 v96, v96, v106, vcc
	v_cmp_class_f32_e32 vcc, v94, v135
	s_nop 1
	v_cndmask_b32_e32 v94, v96, v94, vcc
	v_add_f32_e32 v96, 0x29e12e13, v94
	v_div_scale_f32 v106, s[6:7], v96, v96, 1.0
	v_rcp_f32_e32 v107, v106
	v_mov_b32_e32 v94, 0
	v_cmp_gt_u32_e64 s[6:7], 48, v120
	v_mov_b32_e32 v116, v94
	v_fma_f32 v108, -v106, v107, 1.0
	v_fmac_f32_e32 v107, v108, v107
	v_div_scale_f32 v108, vcc, 1.0, v96, 1.0
	v_mul_f32_e32 v109, v108, v107
	v_fma_f32 v110, -v106, v109, v108
	v_fmac_f32_e32 v109, v110, v107
	v_fma_f32 v106, -v106, v109, v108
	v_div_fmas_f32 v106, v106, v107, v109
	v_div_fixup_f32 v96, v106, v96, 1.0
	v_lshlrev_b32_e32 v106, 3, v123
	v_pk_mul_f32 v[82:83], v[96:97], v[82:83] op_sel_hi:[0,1]
	v_pk_mul_f32 v[84:85], v[96:97], v[84:85] op_sel_hi:[0,1]
	v_pk_mul_f32 v[78:79], v[96:97], v[78:79] op_sel_hi:[0,1]
	v_pk_mul_f32 v[80:81], v[96:97], v[80:81] op_sel_hi:[0,1]
	v_mad_u32_u24 v100, v100, s8, v106
	v_cvt_pk_f16_f32 v82, v82, v83
	v_cvt_pk_f16_f32 v83, v84, v85
	v_cvt_pk_f16_f32 v78, v78, v79
	v_cvt_pk_f16_f32 v79, v80, v81
	ds_write2_b64 v100, v[82:83], v[78:79] offset0:32 offset1:48
	v_pk_mul_f32 v[90:91], v[96:97], v[90:91] op_sel_hi:[0,1]
	v_pk_mul_f32 v[92:93], v[96:97], v[92:93] op_sel_hi:[0,1]
	v_pk_mul_f32 v[86:87], v[96:97], v[86:87] op_sel_hi:[0,1]
	v_pk_mul_f32 v[88:89], v[96:97], v[88:89] op_sel_hi:[0,1]
	v_pk_mul_f32 v[78:79], v[96:97], v[104:105] op_sel_hi:[0,1]
	v_pk_mul_f32 v[80:81], v[96:97], v[102:103] op_sel_hi:[0,1]
	v_sub_u32_e64 v162, v123, 11 clamp
	v_cvt_pk_f16_f32 v90, v90, v91
	v_cvt_pk_f16_f32 v91, v92, v93
	v_cvt_pk_f16_f32 v86, v86, v87
	v_cvt_pk_f16_f32 v87, v88, v89
	v_cvt_pk_f16_f32 v78, v78, v79
	v_cvt_pk_f16_f32 v79, v80, v81
	v_mad_i32_i24 v162, v162, -8, v100
	ds_write2_b64 v100, v[90:91], v[86:87] offset1:16
	ds_write_b64 v162, v[78:79] offset:512
	v_cmp_gt_u32_e64 s[8:9], 24, v120
	v_mov_b32_e32 v96, 0xc604b4df
	v_mov_b32_e32 v95, v94
	v_mov_b32_e32 v98, v94
	v_mov_b32_e32 v99, v94
	v_mov_b32_e32 v100, v94
	v_mov_b32_e32 v101, v94
	v_mov_b32_e32 v102, v94
	v_mov_b32_e32 v103, v94
	v_mov_b32_e32 v104, v94
	v_mov_b32_e32 v105, v94
	v_mov_b32_e32 v106, v94
	v_mov_b32_e32 v107, v94
	v_mov_b32_e32 v108, v94
	v_mov_b32_e32 v109, v94
	v_mov_b32_e32 v110, v94
	v_mov_b32_e32 v111, v94
	v_mov_b32_e32 v112, v94
	v_mov_b32_e32 v113, v94
	v_mov_b32_e32 v114, v94
	v_mov_b32_e32 v115, v94
	v_mov_b32_e32 v117, v94
	s_waitcnt lgkmcnt(0)
	s_barrier
	s_mov_b32 s26, 0x2580
	s_mov_b32 s27, 0x3580
	s_mov_b32 s28, 0x4580
	buffer_load_dwordx4 v[6:9], v192, s[16:19], s26 offen nt
	buffer_load_dwordx4 v[10:13], v192, s[16:19], s26 offen offset:1024 nt
	buffer_load_dwordx4 v[18:21], v192, s[16:19], s26 offen offset:2048 nt
	buffer_load_dwordx4 v[22:25], v192, s[16:19], s26 offen offset:3072 nt
	buffer_load_dwordx4 v[26:29], v192, s[16:19], s27 offen nt
	buffer_load_dwordx4 v[30:33], v192, s[16:19], s27 offen offset:1024 nt
	buffer_load_dwordx4 v[38:41], v192, s[16:19], s27 offen offset:2048 nt
	buffer_load_dwordx4 v[42:45], v192, s[16:19], s27 offen offset:3072 nt
	buffer_load_dwordx4 v[50:53], v192, s[16:19], s28 offen nt
	buffer_load_dwordx4 v[186:189], v193, s[16:19], s26 offen offset:1024 nt
	s_waitcnt vmcnt(25)
	v_cvt_pk_f16_f32 v79, v4, v5
	v_cvt_pk_f16_f32 v78, v2, v3
	ds_write_b64 v141, v[78:79] offset:19456
	s_waitcnt vmcnt(24)
	v_cvt_pk_f16_f32 v79, v16, v17
	v_cvt_pk_f16_f32 v78, v14, v15
	ds_write_b64 v143, v[78:79] offset:19456
	s_waitcnt vmcnt(23)
	v_cvt_pk_f16_f32 v79, v36, v37
	v_cvt_pk_f16_f32 v78, v34, v35
	ds_write_b64 v144, v[78:79] offset:19456
	s_waitcnt vmcnt(22)
	v_cvt_pk_f16_f32 v79, v48, v49
	v_cvt_pk_f16_f32 v78, v46, v47
	ds_write_b64 v145, v[78:79] offset:19456
	s_waitcnt vmcnt(21)
	v_cvt_pk_f16_f32 v79, v56, v57
	v_cvt_pk_f16_f32 v78, v54, v55
	ds_write_b64 v146, v[78:79] offset:19456
	s_waitcnt vmcnt(20)
	v_cvt_pk_f16_f32 v79, v60, v61
	v_cvt_pk_f16_f32 v78, v58, v59
	ds_write_b64 v147, v[78:79] offset:19456
	s_waitcnt vmcnt(19)
	v_cvt_pk_f16_f32 v79, v64, v65
	v_cvt_pk_f16_f32 v78, v62, v63
	ds_write_b64 v141, v[78:79] offset:22568
	s_waitcnt vmcnt(18)
	v_cvt_pk_f16_f32 v79, v68, v69
	v_cvt_pk_f16_f32 v78, v66, v67
	ds_write_b64 v148, v[78:79] offset:19456
	s_waitcnt vmcnt(17)
	v_cvt_pk_f16_f32 v79, v72, v73
	v_cvt_pk_f16_f32 v78, v70, v71
	ds_write_b64 v149, v[78:79] offset:19456
	s_waitcnt vmcnt(16)
	v_cvt_pk_f16_f32 v79, v76, v77
	v_cvt_pk_f16_f32 v78, v74, v75
	s_and_saveexec_b64 s[12:13], s[8:9]
	ds_write_b64 v150, v[78:79] offset:19456
	s_or_b64 exec, exec, s[12:13]
	s_waitcnt vmcnt(10)
	v_cmp_lt_i32_e64 s[30:31], 1, v125
	v_cmp_lt_i32_e64 s[32:33], 1, v190
	v_cmp_lt_i32_e64 s[34:35], 1, v126
	v_cmp_lt_i32_e64 s[36:37], 1, v127
	v_cndmask_b32_e64 v191, 0, 1, s[30:31]
	v_cndmask_b32_e64 v190, 0, 2, s[32:33]
	v_cndmask_b32_e64 v126, 0, 4, s[34:35]
	v_cndmask_b32_e64 v127, 0, 8, s[36:37]
	v_or3_b32 v191, v191, v190, v126
	v_or_b32_e32 v191, v191, v127
	s_mov_b32 s26, 0x4b00
	s_mov_b32 s27, 0x5b00
	s_mov_b32 s28, 0x6b00
	buffer_load_dwordx4 v[2:5], v192, s[16:19], s26 offen nt
	buffer_load_dwordx4 v[14:17], v192, s[16:19], s26 offen offset:1024 nt
	buffer_load_dwordx4 v[34:37], v192, s[16:19], s26 offen offset:2048 nt
	buffer_load_dwordx4 v[46:49], v192, s[16:19], s26 offen offset:3072 nt
	buffer_load_dwordx4 v[54:57], v192, s[16:19], s27 offen nt
	buffer_load_dwordx4 v[58:61], v192, s[16:19], s27 offen offset:1024 nt
	buffer_load_dwordx4 v[62:65], v192, s[16:19], s27 offen offset:2048 nt
	buffer_load_dwordx4 v[66:69], v192, s[16:19], s27 offen offset:3072 nt
	buffer_load_dwordx4 v[70:73], v192, s[16:19], s28 offen nt
	buffer_load_dwordx4 v[74:77], v193, s[16:19], s26 offen offset:1024 nt
	s_mov_b32 s3, 0
	s_branch .LBB0_7
